# RWKV prep waves: the exposed vmcnt wait + identity selects right after each round's next-block prefetch loads removed (loads stay in flight for a block); GEMM unit-boundary peel kept
# baseline (speedup 1.0000x reference)
.LBB0_986:
	s_or_b64 exec, exec, s[94:95]
	s_branch .LBB0_988

.LBB0_993:
	s_or_b64 exec, exec, s[30:31]
	s_branch .LBB0_995
